# weight conversion: nt also on the bf16 weight tile stores of the phase-1 conversion loop
# baseline (speedup 1.0000x reference)
.LBB0_85:
	s_movk_i32 s0, 0x6cf
	v_cmp_lt_i32_e32 vcc, s0, v46
	s_and_saveexec_b64 s[0:1], vcc
	s_xor_b64 s[0:1], exec, s[0:1]
	s_cbranch_execz .LBB0_99
	s_movk_i32 s40, 0x84f
	v_cmp_lt_u32_e32 vcc, s40, v46
	s_and_saveexec_b64 s[42:43], vcc
	s_xor_b64 s[46:47], exec, s[42:43]
	s_cbranch_execz .LBB0_96
	s_movk_i32 s40, 0x94f
	v_cmp_lt_u32_e32 vcc, s40, v46
	s_and_saveexec_b64 s[42:43], vcc
	s_xor_b64 s[48:49], exec, s[42:43]
	s_cbranch_execz .LBB0_93
	s_movk_i32 s42, 0x494f
	v_cmp_lt_u32_e32 vcc, s42, v46
	s_and_saveexec_b64 s[42:43], vcc
	s_xor_b64 s[50:51], exec, s[42:43]
	s_cbranch_execz .LBB0_90
	v_add_u32_e32 v4, 0xffffb6b0, v46
	v_add_u32_e32 v6, 0xffedac00, v3
	v_lshrrev_b32_e32 v130, 9, v4
	v_and_b32_e32 v47, 0x7c0, v6
	v_lshlrev_b64 v[4:5], 23, v[130:131]
	v_and_b32_e32 v76, 0x3c0, v45
	v_or_b32_e32 v7, v47, v123
	v_lshl_add_u64 v[4:5], s[18:19], 0, v[4:5]
	v_lshlrev_b64 v[40:41], 22, v[130:131]
	v_or_b32_e32 v6, v76, v162
	v_lshlrev_b32_e32 v130, 12, v7
	v_lshl_add_u64 v[4:5], v[4:5], 0, v[130:131]
	v_lshlrev_b32_e32 v130, 2, v6
	v_lshl_add_u64 v[68:69], v[4:5], 0, v[130:131]
	s_waitcnt lgkmcnt(0)
	v_add_co_u32_e32 v8, vcc, s88, v68
	s_mov_b32 s41, 0x8000
	s_nop 0
	v_addc_co_u32_e32 v9, vcc, 0, v69, vcc
	v_add_co_u32_e32 v12, vcc, s41, v68
	s_mov_b32 s43, 0x10000
	s_nop 0
	v_addc_co_u32_e32 v13, vcc, 0, v69, vcc
	v_add_co_u32_e32 v16, vcc, s82, v68
	s_mov_b32 s40, 0x14000
	s_nop 0
	v_addc_co_u32_e32 v17, vcc, 0, v69, vcc
	v_add_co_u32_e32 v20, vcc, s43, v68
	s_mov_b32 s42, 0x18000
	s_nop 0
	v_addc_co_u32_e32 v21, vcc, 0, v69, vcc
	v_add_co_u32_e32 v24, vcc, s40, v68
	s_mov_b32 s40, 0x1c000
	s_nop 0
	v_addc_co_u32_e32 v25, vcc, 0, v69, vcc
	v_add_co_u32_e32 v28, vcc, s42, v68
	s_mov_b32 s44, 0x24000
	s_nop 0
	v_addc_co_u32_e32 v29, vcc, 0, v69, vcc
	v_add_co_u32_e32 v32, vcc, s40, v68
	s_mov_b32 s40, 0x20000
	s_nop 0
	v_addc_co_u32_e32 v33, vcc, 0, v69, vcc
	v_add_co_u32_e32 v36, vcc, s40, v68
	s_mov_b32 s45, 0x2c000
	s_nop 0
	v_addc_co_u32_e32 v37, vcc, 0, v69, vcc
	v_add_co_u32_e32 v48, vcc, s44, v68
	s_mov_b32 s44, 0x28000
	s_nop 0
	v_addc_co_u32_e32 v49, vcc, 0, v69, vcc
	v_add_co_u32_e32 v52, vcc, s44, v68
	s_mov_b32 s52, 0x34000
	s_nop 0
	v_addc_co_u32_e32 v53, vcc, 0, v69, vcc
	v_add_co_u32_e32 v56, vcc, s45, v68
	s_mov_b32 s45, 0x30000
	s_nop 0
	v_addc_co_u32_e32 v57, vcc, 0, v69, vcc
	v_add_co_u32_e32 v60, vcc, s45, v68
	global_load_dwordx4 v[4:7], v[68:69], off nt
	s_nop 0
	global_load_dwordx4 v[8:11], v[8:9], off nt
	v_addc_co_u32_e32 v61, vcc, 0, v69, vcc
	v_add_co_u32_e32 v64, vcc, s52, v68
	s_mov_b32 s52, 0x38000
	s_nop 0
	v_addc_co_u32_e32 v65, vcc, 0, v69, vcc
	v_add_co_u32_e32 v70, vcc, s52, v68
	s_mov_b32 s52, 0x3c000
	s_nop 0
	v_addc_co_u32_e32 v71, vcc, 0, v69, vcc
	v_add_co_u32_e32 v72, vcc, s52, v68
	global_load_dwordx4 v[12:15], v[12:13], off nt
	s_nop 0
	global_load_dwordx4 v[16:19], v[16:17], off nt
	v_addc_co_u32_e32 v73, vcc, 0, v69, vcc
	global_load_dwordx4 v[20:23], v[20:21], off nt
	s_nop 0
	global_load_dwordx4 v[24:27], v[24:25], off nt
	s_nop 0
	global_load_dwordx4 v[28:31], v[28:29], off nt
	s_nop 0
	global_load_dwordx4 v[32:35], v[32:33], off nt
	s_nop 0
	global_load_dwordx4 v[36:39], v[36:37], off nt
	s_nop 0
	global_load_dwordx4 v[48:51], v[48:49], off nt
	s_nop 0
	global_load_dwordx4 v[52:55], v[52:53], off nt
	s_nop 0
	global_load_dwordx4 v[56:59], v[56:57], off nt
	s_nop 0
	global_load_dwordx4 v[60:63], v[60:61], off nt
	s_nop 0
	global_load_dwordx4 v[64:67], v[64:65], off nt
	s_nop 0
	global_load_dwordx4 v[68:71], v[70:71], off nt
	s_nop 0
	global_load_dwordx4 v[72:75], v[72:73], off nt
	v_lshl_add_u64 v[40:41], s[78:79], 0, v[40:41]
	s_waitcnt vmcnt(0)
	ds_write2_b32 v163, v4, v5 offset1:1
	ds_write2_b32 v163, v6, v7 offset0:2 offset1:3
	v_add_u32_e32 v4, 0x410, v163
	ds_write2_b32 v4, v8, v9 offset1:1
	v_add_u32_e32 v4, 0x418, v163
	ds_write2_b32 v4, v10, v11 offset1:1
	v_add_u32_e32 v4, 0x820, v163
	ds_write2_b32 v4, v12, v13 offset1:1
	v_add_u32_e32 v4, 0x828, v163
	ds_write2_b32 v4, v14, v15 offset1:1
	v_add_u32_e32 v4, 0xc30, v163
	ds_write2_b32 v4, v16, v17 offset1:1
	v_add_u32_e32 v4, 0xc38, v163
	ds_write2_b32 v4, v18, v19 offset1:1
	v_add_u32_e32 v4, 0x1040, v163
	ds_write2_b32 v4, v20, v21 offset1:1
	v_add_u32_e32 v4, 0x1048, v163
	ds_write2_b32 v4, v22, v23 offset1:1
	v_add_u32_e32 v4, 0x1450, v163
	ds_write2_b32 v4, v24, v25 offset1:1
	v_add_u32_e32 v4, 0x1458, v163
	ds_write2_b32 v4, v26, v27 offset1:1
	v_add_u32_e32 v4, 0x1860, v163
	ds_write2_b32 v4, v28, v29 offset1:1
	v_add_u32_e32 v4, 0x1868, v163
	ds_write2_b32 v4, v30, v31 offset1:1
	v_add_u32_e32 v4, 0x1c70, v163
	ds_write2_b32 v4, v32, v33 offset1:1
	v_add_u32_e32 v4, 0x1c78, v163
	ds_write2_b32 v4, v34, v35 offset1:1
	v_add_u32_e32 v4, 0x2080, v163
	ds_write2_b32 v4, v36, v37 offset1:1
	v_add_u32_e32 v4, 0x2088, v163
	ds_write2_b32 v4, v38, v39 offset1:1
	v_add_u32_e32 v4, 0x2490, v163
	ds_write2_b32 v4, v48, v49 offset1:1
	v_add_u32_e32 v4, 0x2498, v163
	ds_write2_b32 v4, v50, v51 offset1:1
	v_add_u32_e32 v4, 0x28a0, v163
	ds_write2_b32 v4, v52, v53 offset1:1
	v_add_u32_e32 v4, 0x28a8, v163
	ds_write2_b32 v4, v54, v55 offset1:1
	v_add_u32_e32 v4, 0x2cb0, v163
	ds_write2_b32 v4, v56, v57 offset1:1
	v_add_u32_e32 v4, 0x2cb8, v163
	ds_write2_b32 v4, v58, v59 offset1:1
	v_add_u32_e32 v4, 0x30c0, v163
	ds_write2_b32 v4, v60, v61 offset1:1
	v_add_u32_e32 v4, 0x30c8, v163
	ds_write2_b32 v4, v62, v63 offset1:1
	v_add_u32_e32 v4, 0x34d0, v163
	ds_write2_b32 v4, v64, v65 offset1:1
	v_add_u32_e32 v4, 0x34d8, v163
	ds_write2_b32 v4, v66, v67 offset1:1
	v_add_u32_e32 v4, 0x38e0, v163
	ds_write2_b32 v4, v68, v69 offset1:1
	v_add_u32_e32 v4, 0x38e8, v163
	ds_write2_b32 v4, v70, v71 offset1:1
	v_add_u32_e32 v4, 0x3cf0, v163
	ds_write2_b32 v4, v72, v73 offset1:1
	v_add_u32_e32 v4, 0x3cf8, v163
	ds_write2_b32 v4, v74, v75 offset1:1
	v_add_u32_e32 v49, 0x400, v165
	ds_read2_b32 v[8:9], v165 offset0:65 offset1:73
	ds_read2_b32 v[10:11], v165 offset0:130 offset1:138
	ds_read2_b32 v[12:13], v165 offset0:195 offset1:203
	ds_read2_b32 v[14:15], v49 offset0:4 offset1:12
	ds_read2_b32 v[16:17], v49 offset0:69 offset1:77
	ds_read2_b32 v[18:19], v49 offset0:134 offset1:142
	ds_read2_b32 v[20:21], v49 offset0:199 offset1:207
	ds_read2_b32 v[22:23], v165 offset1:8
	ds_read2_b32 v[24:25], v165 offset0:16 offset1:24
	ds_read2_b32 v[26:27], v165 offset0:81 offset1:89
	ds_read2_b32 v[28:29], v165 offset0:146 offset1:154
	ds_read2_b32 v[30:31], v165 offset0:211 offset1:219
	ds_read2_b32 v[32:33], v49 offset0:20 offset1:28
	ds_read2_b32 v[34:35], v49 offset0:85 offset1:93
	ds_read2_b32 v[36:37], v49 offset0:150 offset1:158
	ds_read2_b32 v[38:39], v49 offset0:215 offset1:223
	v_lshlrev_b32_e32 v130, 1, v47
	v_lshl_add_u64 v[4:5], v[40:41], 0, v[130:131]
	v_lshlrev_b32_e32 v130, 1, v116
	v_or_b32_e32 v48, v76, v164
	v_lshl_add_u64 v[40:41], v[4:5], 0, v[130:131]
	v_lshlrev_b32_e32 v130, 12, v48
	v_lshl_add_u64 v[40:41], v[40:41], 0, v[130:131]
	s_waitcnt lgkmcnt(8)
	v_cvt_pk_bf16_f32 v4, v22, v8
	v_cvt_pk_bf16_f32 v5, v10, v12
	v_cvt_pk_bf16_f32 v6, v14, v16
	v_cvt_pk_bf16_f32 v7, v18, v20
	v_add_co_u32_e32 v8, vcc, s41, v40
	global_store_dwordx4 v[40:41], v[4:7], off nt
	s_mov_b32 s77, 0x8000
	s_mov_b32 s80, 0x10000
	v_cvt_pk_bf16_f32 v4, v23, v9
	v_cvt_pk_bf16_f32 v5, v11, v13
	v_cvt_pk_bf16_f32 v6, v15, v17
	v_cvt_pk_bf16_f32 v7, v19, v21
	v_addc_co_u32_e32 v9, vcc, 0, v41, vcc
	global_store_dwordx4 v[8:9], v[4:7], off nt
	v_add_co_u32_e32 v8, vcc, s43, v40
	s_waitcnt lgkmcnt(6)
	v_cvt_pk_bf16_f32 v4, v24, v26
	s_waitcnt lgkmcnt(4)
	v_cvt_pk_bf16_f32 v5, v28, v30
	s_waitcnt lgkmcnt(2)
	v_cvt_pk_bf16_f32 v6, v32, v34
	s_waitcnt lgkmcnt(0)
	v_cvt_pk_bf16_f32 v7, v36, v38
	v_addc_co_u32_e32 v9, vcc, 0, v41, vcc
	global_store_dwordx4 v[8:9], v[4:7], off nt
	v_add_co_u32_e32 v48, vcc, s42, v40
	s_nop 0
	v_cvt_pk_bf16_f32 v4, v25, v27
	v_cvt_pk_bf16_f32 v5, v29, v31
	v_cvt_pk_bf16_f32 v6, v33, v35
	v_cvt_pk_bf16_f32 v7, v37, v39
	ds_read2_b32 v[8:9], v165 offset0:97 offset1:105
	ds_read2_b32 v[10:11], v165 offset0:162 offset1:170
	ds_read2_b32 v[12:13], v165 offset0:227 offset1:235
	ds_read2_b32 v[14:15], v49 offset0:36 offset1:44
	ds_read2_b32 v[16:17], v49 offset0:101 offset1:109
	ds_read2_b32 v[18:19], v49 offset0:166 offset1:174
	ds_read2_b32 v[20:21], v49 offset0:231 offset1:239
	ds_read2_b32 v[22:23], v165 offset0:32 offset1:40
	ds_read2_b32 v[24:25], v165 offset0:48 offset1:56
	ds_read2_b32 v[26:27], v165 offset0:113 offset1:121
	ds_read2_b32 v[28:29], v165 offset0:178 offset1:186
	ds_read2_b32 v[30:31], v165 offset0:243 offset1:251
	ds_read2_b32 v[32:33], v49 offset0:52 offset1:60
	ds_read2_b32 v[34:35], v49 offset0:117 offset1:125
	ds_read2_b32 v[36:37], v49 offset0:182 offset1:190
	ds_read2_b32 v[38:39], v49 offset0:247 offset1:255
	s_mov_b32 s83, 0x18000
	v_addc_co_u32_e32 v49, vcc, 0, v41, vcc
	global_store_dwordx4 v[48:49], v[4:7], off nt
	v_add_co_u32_e32 v48, vcc, s40, v40
	s_waitcnt lgkmcnt(8)
	v_cvt_pk_bf16_f32 v4, v22, v8
	v_addc_co_u32_e32 v49, vcc, 0, v41, vcc
	v_cvt_pk_bf16_f32 v5, v10, v12
	v_cvt_pk_bf16_f32 v6, v14, v16
	v_cvt_pk_bf16_f32 v7, v18, v20
	v_add_co_u32_e32 v8, vcc, s44, v40
	global_store_dwordx4 v[48:49], v[4:7], off nt
	s_nop 1
	v_cvt_pk_bf16_f32 v4, v23, v9
	v_cvt_pk_bf16_f32 v5, v11, v13
	v_cvt_pk_bf16_f32 v6, v15, v17
	v_cvt_pk_bf16_f32 v7, v19, v21
	v_addc_co_u32_e32 v9, vcc, 0, v41, vcc
	global_store_dwordx4 v[8:9], v[4:7], off nt
	v_add_co_u32_e32 v8, vcc, s45, v40
	s_waitcnt lgkmcnt(6)
	v_cvt_pk_bf16_f32 v4, v24, v26
	s_waitcnt lgkmcnt(4)
	v_cvt_pk_bf16_f32 v5, v28, v30
	s_waitcnt lgkmcnt(2)
	v_cvt_pk_bf16_f32 v6, v32, v34
	s_waitcnt lgkmcnt(0)
	v_cvt_pk_bf16_f32 v7, v36, v38
	v_addc_co_u32_e32 v9, vcc, 0, v41, vcc
	global_store_dwordx4 v[8:9], v[4:7], off nt
	v_add_co_u32_e32 v8, vcc, 0x38000, v40
	s_nop 0
	v_cvt_pk_bf16_f32 v4, v25, v27
	v_cvt_pk_bf16_f32 v5, v29, v31
	v_cvt_pk_bf16_f32 v6, v33, v35
	v_cvt_pk_bf16_f32 v7, v37, v39
	v_addc_co_u32_e32 v9, vcc, 0, v41, vcc
	global_store_dwordx4 v[8:9], v[4:7], off nt
.LBB0_90:
	s_andn2_saveexec_b64 s[50:51], s[50:51]
	s_cbranch_execz .LBB0_92
	v_add_u32_e32 v47, 0xfffff6b0, v46
	v_mov_b32_e32 v4, s67
	v_mov_b32_e32 v5, s65
	v_cmp_gt_u32_e32 vcc, s76, v47
	v_mov_b32_e32 v6, s64
	v_readlane_b32 s40, v255, 30
	v_cndmask_b32_e32 v5, v4, v5, vcc
	v_mov_b32_e32 v4, s66
	v_cndmask_b32_e32 v4, v4, v6, vcc
	v_and_b32_e32 v130, 0x7800000, v44
	v_and_b32_e32 v76, 0x3c0, v3
	v_readlane_b32 s41, v255, 31
	v_lshl_add_u64 v[4:5], v[4:5], 0, s[16:17]
	v_add_u32_e32 v77, 0xffffdac0, v42
	v_lshl_add_u64 v[40:41], s[40:41], 0, v[130:131]
	s_movk_i32 s40, 0x7c0
	v_or_b32_e32 v7, v76, v123
	v_lshl_add_u64 v[4:5], v[4:5], 0, v[130:131]
	v_and_or_b32 v6, v77, s40, v162
	v_lshlrev_b32_e32 v130, 13, v7
	v_lshl_add_u64 v[4:5], v[4:5], 0, v[130:131]
	v_lshlrev_b32_e32 v130, 2, v6
	v_lshl_add_u64 v[68:69], v[4:5], 0, v[130:131]
	s_mov_b32 s41, 0x8000
	s_waitcnt lgkmcnt(0)
	v_add_co_u32_e32 v8, vcc, s41, v68
	s_mov_b32 s43, 0x10000
	s_nop 0
	v_addc_co_u32_e32 v9, vcc, 0, v69, vcc
	v_add_co_u32_e32 v12, vcc, s43, v68
	s_mov_b32 s42, 0x18000
	s_nop 0
	v_addc_co_u32_e32 v13, vcc, 0, v69, vcc
	v_add_co_u32_e32 v16, vcc, s42, v68
	s_mov_b32 s40, 0x20000
	s_nop 0
	v_addc_co_u32_e32 v17, vcc, 0, v69, vcc
	v_add_co_u32_e32 v20, vcc, s40, v68
	s_mov_b32 s40, 0x28000
	s_nop 0
	v_addc_co_u32_e32 v21, vcc, 0, v69, vcc
	v_add_co_u32_e32 v24, vcc, s40, v68
	s_mov_b32 s40, 0x30000
	s_nop 0
	v_addc_co_u32_e32 v25, vcc, 0, v69, vcc
	v_add_co_u32_e32 v28, vcc, s40, v68
	s_mov_b32 s40, 0x38000
	s_nop 0
	v_addc_co_u32_e32 v29, vcc, 0, v69, vcc
	v_add_co_u32_e32 v32, vcc, s40, v68
	s_mov_b32 s40, 0x40000
	s_nop 0
	v_addc_co_u32_e32 v33, vcc, 0, v69, vcc
	v_add_co_u32_e32 v36, vcc, s40, v68
	s_mov_b32 s40, 0x48000
	s_nop 0
	v_addc_co_u32_e32 v37, vcc, 0, v69, vcc
	v_add_co_u32_e32 v48, vcc, s40, v68
	s_mov_b32 s40, 0x50000
	s_nop 0
	v_addc_co_u32_e32 v49, vcc, 0, v69, vcc
	v_add_co_u32_e32 v52, vcc, s40, v68
	s_mov_b32 s40, 0x58000
	s_nop 0
	v_addc_co_u32_e32 v53, vcc, 0, v69, vcc
	v_add_co_u32_e32 v56, vcc, s40, v68
	s_mov_b32 s40, 0x60000
	s_nop 0
	v_addc_co_u32_e32 v57, vcc, 0, v69, vcc
	v_add_co_u32_e32 v60, vcc, s40, v68
	s_mov_b32 s40, 0x68000
	s_nop 0
	v_addc_co_u32_e32 v61, vcc, 0, v69, vcc
	v_add_co_u32_e32 v64, vcc, s40, v68
	s_mov_b32 s40, 0x70000
	s_nop 0
	v_addc_co_u32_e32 v65, vcc, 0, v69, vcc
	v_add_co_u32_e32 v70, vcc, s40, v68
	s_mov_b32 s40, 0x78000
	s_nop 0
	v_addc_co_u32_e32 v71, vcc, 0, v69, vcc
	v_add_co_u32_e32 v72, vcc, s40, v68
	global_load_dwordx4 v[4:7], v[68:69], off nt
	s_nop 0
	global_load_dwordx4 v[8:11], v[8:9], off nt
	v_addc_co_u32_e32 v73, vcc, 0, v69, vcc
	global_load_dwordx4 v[12:15], v[12:13], off nt
	s_nop 0
	global_load_dwordx4 v[16:19], v[16:17], off nt
	s_nop 0
	global_load_dwordx4 v[20:23], v[20:21], off nt
	s_nop 0
	global_load_dwordx4 v[24:27], v[24:25], off nt
	s_nop 0
	global_load_dwordx4 v[28:31], v[28:29], off nt
	s_nop 0
	global_load_dwordx4 v[32:35], v[32:33], off nt
	s_nop 0
	global_load_dwordx4 v[36:39], v[36:37], off nt
	s_nop 0
	global_load_dwordx4 v[48:51], v[48:49], off nt
	s_nop 0
	global_load_dwordx4 v[52:55], v[52:53], off nt
	s_nop 0
	global_load_dwordx4 v[56:59], v[56:57], off nt
	s_nop 0
	global_load_dwordx4 v[60:63], v[60:61], off nt
	s_nop 0
	global_load_dwordx4 v[64:67], v[64:65], off nt
	s_nop 0
	global_load_dwordx4 v[68:71], v[70:71], off nt
	s_nop 0
	global_load_dwordx4 v[72:75], v[72:73], off nt
	s_waitcnt vmcnt(0)
	ds_write2_b32 v163, v4, v5 offset1:1
	ds_write2_b32 v163, v6, v7 offset0:2 offset1:3
	v_add_u32_e32 v4, 0x410, v163
	ds_write2_b32 v4, v8, v9 offset1:1
	v_add_u32_e32 v4, 0x418, v163
	ds_write2_b32 v4, v10, v11 offset1:1
	v_add_u32_e32 v4, 0x820, v163
	ds_write2_b32 v4, v12, v13 offset1:1
	v_add_u32_e32 v4, 0x828, v163
	ds_write2_b32 v4, v14, v15 offset1:1
	v_add_u32_e32 v4, 0xc30, v163
	ds_write2_b32 v4, v16, v17 offset1:1
	v_add_u32_e32 v4, 0xc38, v163
	ds_write2_b32 v4, v18, v19 offset1:1
	v_add_u32_e32 v4, 0x1040, v163
	ds_write2_b32 v4, v20, v21 offset1:1
	v_add_u32_e32 v4, 0x1048, v163
	ds_write2_b32 v4, v22, v23 offset1:1
	v_add_u32_e32 v4, 0x1450, v163
	ds_write2_b32 v4, v24, v25 offset1:1
	v_add_u32_e32 v4, 0x1458, v163
	ds_write2_b32 v4, v26, v27 offset1:1
	v_add_u32_e32 v4, 0x1860, v163
	ds_write2_b32 v4, v28, v29 offset1:1
	v_add_u32_e32 v4, 0x1868, v163
	ds_write2_b32 v4, v30, v31 offset1:1
	v_add_u32_e32 v4, 0x1c70, v163
	ds_write2_b32 v4, v32, v33 offset1:1
	v_add_u32_e32 v4, 0x1c78, v163
	ds_write2_b32 v4, v34, v35 offset1:1
	v_add_u32_e32 v4, 0x2080, v163
	ds_write2_b32 v4, v36, v37 offset1:1
	v_add_u32_e32 v4, 0x2088, v163
	ds_write2_b32 v4, v38, v39 offset1:1
	v_add_u32_e32 v4, 0x2490, v163
	ds_write2_b32 v4, v48, v49 offset1:1
	v_add_u32_e32 v4, 0x2498, v163
	ds_write2_b32 v4, v50, v51 offset1:1
	v_add_u32_e32 v4, 0x28a0, v163
	ds_write2_b32 v4, v52, v53 offset1:1
	v_add_u32_e32 v4, 0x28a8, v163
	ds_write2_b32 v4, v54, v55 offset1:1
	v_add_u32_e32 v4, 0x2cb0, v163
	ds_write2_b32 v4, v56, v57 offset1:1
	v_add_u32_e32 v4, 0x2cb8, v163
	ds_write2_b32 v4, v58, v59 offset1:1
	v_add_u32_e32 v4, 0x30c0, v163
	ds_write2_b32 v4, v60, v61 offset1:1
	v_add_u32_e32 v4, 0x30c8, v163
	ds_write2_b32 v4, v62, v63 offset1:1
	v_add_u32_e32 v4, 0x34d0, v163
	ds_write2_b32 v4, v64, v65 offset1:1
	v_add_u32_e32 v4, 0x34d8, v163
	ds_write2_b32 v4, v66, v67 offset1:1
	v_add_u32_e32 v4, 0x38e0, v163
	ds_write2_b32 v4, v68, v69 offset1:1
	v_add_u32_e32 v4, 0x38e8, v163
	ds_write2_b32 v4, v70, v71 offset1:1
	v_add_u32_e32 v4, 0x3cf0, v163
	ds_write2_b32 v4, v72, v73 offset1:1
	v_add_u32_e32 v4, 0x3cf8, v163
	s_movk_i32 s40, 0x1fff
	ds_write2_b32 v4, v74, v75 offset1:1
	v_cmp_lt_u32_e32 vcc, s40, v47
	v_add_u32_e32 v47, 0x400, v165
	ds_read2_b32 v[8:9], v165 offset0:65 offset1:73
	ds_read2_b32 v[10:11], v165 offset0:130 offset1:138
	ds_read2_b32 v[12:13], v165 offset0:195 offset1:203
	ds_read2_b32 v[14:15], v47 offset0:4 offset1:12
	ds_read2_b32 v[16:17], v47 offset0:69 offset1:77
	ds_read2_b32 v[18:19], v47 offset0:134 offset1:142
	ds_read2_b32 v[20:21], v47 offset0:199 offset1:207
	ds_read2_b32 v[22:23], v165 offset1:8
	ds_read2_b32 v[24:25], v165 offset0:16 offset1:24
	ds_read2_b32 v[26:27], v165 offset0:81 offset1:89
	ds_read2_b32 v[28:29], v165 offset0:146 offset1:154
	ds_read2_b32 v[30:31], v165 offset0:211 offset1:219
	ds_read2_b32 v[32:33], v47 offset0:20 offset1:28
	ds_read2_b32 v[34:35], v47 offset0:85 offset1:93
	ds_read2_b32 v[36:37], v47 offset0:150 offset1:158
	ds_read2_b32 v[38:39], v47 offset0:215 offset1:223
	v_lshlrev_b32_e32 v130, 1, v76
	v_lshl_add_u64 v[4:5], v[40:41], 0, v[130:131]
	v_lshlrev_b32_e32 v130, 1, v116
	v_cndmask_b32_e32 v6, 0, v229, vcc
	v_lshl_add_u64 v[40:41], v[4:5], 0, v[130:131]
	v_lshlrev_b32_e32 v4, 1, v77
	v_and_b32_e32 v4, 0xf00, v4
	v_and_or_b32 v5, v77, 64, v6
	v_or3_b32 v48, v5, v4, v164
	v_lshlrev_b32_e32 v130, 11, v48
	v_lshl_add_u64 v[40:41], v[40:41], 0, v[130:131]
	s_waitcnt lgkmcnt(8)
	v_cvt_pk_bf16_f32 v4, v22, v8
	v_cvt_pk_bf16_f32 v5, v10, v12
	v_cvt_pk_bf16_f32 v6, v14, v16
	v_cvt_pk_bf16_f32 v7, v18, v20
	v_add_co_u32_e32 v8, vcc, s88, v40
	global_store_dwordx4 v[40:41], v[4:7], off nt
	s_mov_b32 s77, 0x8000
	s_nop 0
	v_cvt_pk_bf16_f32 v4, v23, v9
	v_cvt_pk_bf16_f32 v5, v11, v13
	v_cvt_pk_bf16_f32 v6, v15, v17
	v_cvt_pk_bf16_f32 v7, v19, v21
	v_addc_co_u32_e32 v9, vcc, 0, v41, vcc
	global_store_dwordx4 v[8:9], v[4:7], off nt
	v_add_co_u32_e32 v8, vcc, s41, v40
	s_waitcnt lgkmcnt(6)
	v_cvt_pk_bf16_f32 v4, v24, v26
	s_waitcnt lgkmcnt(4)
	v_cvt_pk_bf16_f32 v5, v28, v30
	s_waitcnt lgkmcnt(2)
	v_cvt_pk_bf16_f32 v6, v32, v34
	s_waitcnt lgkmcnt(0)
	v_cvt_pk_bf16_f32 v7, v36, v38
	v_addc_co_u32_e32 v9, vcc, 0, v41, vcc
	global_store_dwordx4 v[8:9], v[4:7], off nt
	v_add_co_u32_e32 v48, vcc, s82, v40
	s_nop 0
	v_cvt_pk_bf16_f32 v4, v25, v27
	v_cvt_pk_bf16_f32 v5, v29, v31
	v_cvt_pk_bf16_f32 v6, v33, v35
	v_cvt_pk_bf16_f32 v7, v37, v39
	ds_read2_b32 v[8:9], v165 offset0:97 offset1:105
	ds_read2_b32 v[10:11], v165 offset0:162 offset1:170
	ds_read2_b32 v[12:13], v165 offset0:227 offset1:235
	ds_read2_b32 v[14:15], v47 offset0:36 offset1:44
	ds_read2_b32 v[16:17], v47 offset0:101 offset1:109
	ds_read2_b32 v[18:19], v47 offset0:166 offset1:174
	ds_read2_b32 v[20:21], v47 offset0:231 offset1:239
	ds_read2_b32 v[22:23], v165 offset0:32 offset1:40
	ds_read2_b32 v[24:25], v165 offset0:48 offset1:56
	ds_read2_b32 v[26:27], v165 offset0:113 offset1:121
	ds_read2_b32 v[28:29], v165 offset0:178 offset1:186
	ds_read2_b32 v[30:31], v165 offset0:243 offset1:251
	ds_read2_b32 v[32:33], v47 offset0:52 offset1:60
	ds_read2_b32 v[34:35], v47 offset0:117 offset1:125
	ds_read2_b32 v[36:37], v47 offset0:182 offset1:190
	ds_read2_b32 v[38:39], v47 offset0:247 offset1:255
	v_addc_co_u32_e32 v49, vcc, 0, v41, vcc
	global_store_dwordx4 v[48:49], v[4:7], off nt
	v_add_co_u32_e32 v48, vcc, s43, v40
	s_mov_b32 s40, 0x14000
	s_nop 0
	v_addc_co_u32_e32 v49, vcc, 0, v41, vcc
	s_waitcnt lgkmcnt(8)
	v_cvt_pk_bf16_f32 v4, v22, v8
	v_cvt_pk_bf16_f32 v5, v10, v12
	v_cvt_pk_bf16_f32 v6, v14, v16
	v_cvt_pk_bf16_f32 v7, v18, v20
	v_add_co_u32_e32 v8, vcc, s40, v40
	global_store_dwordx4 v[48:49], v[4:7], off nt
	s_mov_b32 s80, 0x10000
	s_mov_b32 s83, 0x18000
	v_cvt_pk_bf16_f32 v4, v23, v9
	v_cvt_pk_bf16_f32 v5, v11, v13
	v_cvt_pk_bf16_f32 v6, v15, v17
	v_cvt_pk_bf16_f32 v7, v19, v21
	v_addc_co_u32_e32 v9, vcc, 0, v41, vcc
	global_store_dwordx4 v[8:9], v[4:7], off nt
	v_add_co_u32_e32 v8, vcc, s42, v40
	s_waitcnt lgkmcnt(6)
	v_cvt_pk_bf16_f32 v4, v24, v26
	s_waitcnt lgkmcnt(4)
	v_cvt_pk_bf16_f32 v5, v28, v30
	s_waitcnt lgkmcnt(2)
	v_cvt_pk_bf16_f32 v6, v32, v34
	s_waitcnt lgkmcnt(0)
	v_cvt_pk_bf16_f32 v7, v36, v38
	v_addc_co_u32_e32 v9, vcc, 0, v41, vcc
	global_store_dwordx4 v[8:9], v[4:7], off nt
	v_add_co_u32_e32 v8, vcc, 0x1c000, v40
	s_nop 0
	v_cvt_pk_bf16_f32 v4, v25, v27
	v_cvt_pk_bf16_f32 v5, v29, v31
	v_cvt_pk_bf16_f32 v6, v33, v35
	v_cvt_pk_bf16_f32 v7, v37, v39
	v_addc_co_u32_e32 v9, vcc, 0, v41, vcc
	global_store_dwordx4 v[8:9], v[4:7], off nt

.LBB0_93:
	s_andn2_saveexec_b64 s[48:49], s[48:49]
	s_cbranch_execz .LBB0_95
	v_and_b32_e32 v47, 0x3c0, v3
	v_and_b32_e32 v4, 0x3fc0, v42
	v_or_b32_e32 v5, v47, v123
	v_add_u32_e32 v76, 0xffffdec0, v4
	v_lshlrev_b32_e32 v130, 12, v5
	v_or_b32_e32 v4, v76, v162
	v_lshl_add_u64 v[6:7], s[20:21], 0, v[130:131]
	v_mov_b32_e32 v5, v131
	v_lshl_add_u64 v[40:41], v[4:5], 2, v[6:7]
	s_waitcnt lgkmcnt(0)
	v_add_co_u32_e32 v8, vcc, 0x4000, v40
	s_mov_b32 s40, 0x20000
	s_nop 0
	v_addc_co_u32_e32 v9, vcc, 0, v41, vcc
	v_add_co_u32_e32 v12, vcc, 0x8000, v40
	global_load_dwordx4 v[4:7], v[40:41], off nt
	s_nop 0
	global_load_dwordx4 v[8:11], v[8:9], off nt
	v_addc_co_u32_e32 v13, vcc, 0, v41, vcc
	v_add_co_u32_e32 v16, vcc, 0xc000, v40
	s_nop 1
	v_addc_co_u32_e32 v17, vcc, 0, v41, vcc
	v_add_co_u32_e32 v20, vcc, 0x10000, v40
	global_load_dwordx4 v[12:15], v[12:13], off nt
	s_nop 0
	global_load_dwordx4 v[16:19], v[16:17], off nt
	v_addc_co_u32_e32 v21, vcc, 0, v41, vcc
	v_add_co_u32_e32 v24, vcc, 0x14000, v40
	s_nop 1
	v_addc_co_u32_e32 v25, vcc, 0, v41, vcc
	v_add_co_u32_e32 v28, vcc, 0x18000, v40
	global_load_dwordx4 v[20:23], v[20:21], off nt
	s_nop 0
	global_load_dwordx4 v[24:27], v[24:25], off nt
	v_addc_co_u32_e32 v29, vcc, 0, v41, vcc
	v_add_co_u32_e32 v32, vcc, 0x1c000, v40
	s_nop 1
	v_addc_co_u32_e32 v33, vcc, 0, v41, vcc
	v_add_co_u32_e32 v36, vcc, s40, v40
	global_load_dwordx4 v[28:31], v[28:29], off nt
	s_nop 0
	global_load_dwordx4 v[32:35], v[32:33], off nt
	v_addc_co_u32_e32 v37, vcc, 0, v41, vcc
	v_add_co_u32_e32 v48, vcc, 0x24000, v40
	s_nop 1
	v_addc_co_u32_e32 v49, vcc, 0, v41, vcc
	v_add_co_u32_e32 v52, vcc, 0x28000, v40
	global_load_dwordx4 v[36:39], v[36:37], off nt
	s_nop 0
	global_load_dwordx4 v[48:51], v[48:49], off nt
	v_addc_co_u32_e32 v53, vcc, 0, v41, vcc
	v_add_co_u32_e32 v56, vcc, 0x2c000, v40
	s_nop 1
	v_addc_co_u32_e32 v57, vcc, 0, v41, vcc
	v_add_co_u32_e32 v60, vcc, 0x30000, v40
	global_load_dwordx4 v[52:55], v[52:53], off nt
	s_nop 0
	global_load_dwordx4 v[56:59], v[56:57], off nt
	v_addc_co_u32_e32 v61, vcc, 0, v41, vcc
	v_add_co_u32_e32 v64, vcc, 0x34000, v40
	s_nop 1
	v_addc_co_u32_e32 v65, vcc, 0, v41, vcc
	v_add_co_u32_e32 v68, vcc, 0x38000, v40
	global_load_dwordx4 v[60:63], v[60:61], off nt
	s_nop 0
	global_load_dwordx4 v[64:67], v[64:65], off nt
	v_addc_co_u32_e32 v69, vcc, 0, v41, vcc
	v_add_co_u32_e32 v40, vcc, 0x3c000, v40
	s_nop 1
	v_addc_co_u32_e32 v41, vcc, 0, v41, vcc
	global_load_dwordx4 v[68:71], v[68:69], off nt
	s_nop 0
	global_load_dwordx4 v[72:75], v[40:41], off nt
	s_waitcnt vmcnt(0)
	ds_write2_b32 v163, v4, v5 offset1:1
	ds_write2_b32 v163, v6, v7 offset0:2 offset1:3
	v_add_u32_e32 v4, 0x410, v163
	ds_write2_b32 v4, v8, v9 offset1:1
	v_add_u32_e32 v4, 0x418, v163
	ds_write2_b32 v4, v10, v11 offset1:1
	v_add_u32_e32 v4, 0x820, v163
	ds_write2_b32 v4, v12, v13 offset1:1
	v_add_u32_e32 v4, 0x828, v163
	ds_write2_b32 v4, v14, v15 offset1:1
	v_add_u32_e32 v4, 0xc30, v163
	ds_write2_b32 v4, v16, v17 offset1:1
	v_add_u32_e32 v4, 0xc38, v163
	ds_write2_b32 v4, v18, v19 offset1:1
	v_add_u32_e32 v4, 0x1040, v163
	ds_write2_b32 v4, v20, v21 offset1:1
	v_add_u32_e32 v4, 0x1048, v163
	ds_write2_b32 v4, v22, v23 offset1:1
	v_add_u32_e32 v4, 0x1450, v163
	ds_write2_b32 v4, v24, v25 offset1:1
	v_add_u32_e32 v4, 0x1458, v163
	ds_write2_b32 v4, v26, v27 offset1:1
	v_add_u32_e32 v4, 0x1860, v163
	ds_write2_b32 v4, v28, v29 offset1:1
	v_add_u32_e32 v4, 0x1868, v163
	ds_write2_b32 v4, v30, v31 offset1:1
	v_add_u32_e32 v4, 0x1c70, v163
	ds_write2_b32 v4, v32, v33 offset1:1
	v_add_u32_e32 v4, 0x1c78, v163
	ds_write2_b32 v4, v34, v35 offset1:1
	v_add_u32_e32 v4, 0x2080, v163
	ds_write2_b32 v4, v36, v37 offset1:1
	v_add_u32_e32 v4, 0x2088, v163
	ds_write2_b32 v4, v38, v39 offset1:1
	v_add_u32_e32 v4, 0x2490, v163
	ds_write2_b32 v4, v48, v49 offset1:1
	v_add_u32_e32 v4, 0x2498, v163
	ds_write2_b32 v4, v50, v51 offset1:1
	v_add_u32_e32 v4, 0x28a0, v163
	ds_write2_b32 v4, v52, v53 offset1:1
	v_add_u32_e32 v4, 0x28a8, v163
	ds_write2_b32 v4, v54, v55 offset1:1
	v_add_u32_e32 v4, 0x2cb0, v163
	ds_write2_b32 v4, v56, v57 offset1:1
	v_add_u32_e32 v4, 0x2cb8, v163
	ds_write2_b32 v4, v58, v59 offset1:1
	v_add_u32_e32 v4, 0x30c0, v163
	ds_write2_b32 v4, v60, v61 offset1:1
	v_add_u32_e32 v4, 0x30c8, v163
	ds_write2_b32 v4, v62, v63 offset1:1
	v_add_u32_e32 v4, 0x34d0, v163
	ds_write2_b32 v4, v64, v65 offset1:1
	v_add_u32_e32 v4, 0x34d8, v163
	ds_write2_b32 v4, v66, v67 offset1:1
	v_add_u32_e32 v4, 0x38e0, v163
	ds_write2_b32 v4, v68, v69 offset1:1
	v_add_u32_e32 v4, 0x38e8, v163
	ds_write2_b32 v4, v70, v71 offset1:1
	v_add_u32_e32 v4, 0x3cf0, v163
	ds_write2_b32 v4, v72, v73 offset1:1
	v_add_u32_e32 v4, 0x3cf8, v163
	ds_write2_b32 v4, v74, v75 offset1:1
	v_add_u32_e32 v48, 0x400, v165
	ds_read2_b32 v[8:9], v165 offset0:65 offset1:73
	ds_read2_b32 v[10:11], v165 offset0:130 offset1:138
	ds_read2_b32 v[12:13], v165 offset0:195 offset1:203
	ds_read2_b32 v[14:15], v48 offset0:4 offset1:12
	ds_read2_b32 v[16:17], v48 offset0:69 offset1:77
	ds_read2_b32 v[18:19], v48 offset0:134 offset1:142
	ds_read2_b32 v[20:21], v48 offset0:199 offset1:207
	ds_read2_b32 v[22:23], v165 offset1:8
	ds_read2_b32 v[24:25], v165 offset0:16 offset1:24
	ds_read2_b32 v[26:27], v165 offset0:81 offset1:89
	ds_read2_b32 v[28:29], v165 offset0:146 offset1:154
	ds_read2_b32 v[30:31], v165 offset0:211 offset1:219
	ds_read2_b32 v[32:33], v48 offset0:20 offset1:28
	ds_read2_b32 v[34:35], v48 offset0:85 offset1:93
	ds_read2_b32 v[36:37], v48 offset0:150 offset1:158
	ds_read2_b32 v[38:39], v48 offset0:215 offset1:223
	v_lshlrev_b32_e32 v130, 1, v47
	v_or_b32_e32 v49, v76, v164
	v_lshl_add_u64 v[40:41], v[118:119], 0, v[130:131]
	v_lshlrev_b32_e32 v130, 11, v49
	v_lshl_add_u64 v[40:41], v[40:41], 0, v[130:131]
	s_waitcnt lgkmcnt(8)
	v_cvt_pk_bf16_f32 v4, v22, v8
	v_cvt_pk_bf16_f32 v5, v10, v12
	v_cvt_pk_bf16_f32 v6, v14, v16
	v_cvt_pk_bf16_f32 v7, v18, v20
	v_add_co_u32_e32 v8, vcc, s88, v40
	global_store_dwordx4 v[40:41], v[4:7], off nt
	s_nop 1
	v_cvt_pk_bf16_f32 v4, v23, v9
	v_cvt_pk_bf16_f32 v5, v11, v13
	v_cvt_pk_bf16_f32 v6, v15, v17
	v_cvt_pk_bf16_f32 v7, v19, v21
	v_addc_co_u32_e32 v9, vcc, 0, v41, vcc
	global_store_dwordx4 v[8:9], v[4:7], off nt
	v_add_co_u32_e32 v8, vcc, s77, v40
	s_waitcnt lgkmcnt(6)
	v_cvt_pk_bf16_f32 v4, v24, v26
	s_waitcnt lgkmcnt(4)
	v_cvt_pk_bf16_f32 v5, v28, v30
	s_waitcnt lgkmcnt(2)
	v_cvt_pk_bf16_f32 v6, v32, v34
	s_waitcnt lgkmcnt(0)
	v_cvt_pk_bf16_f32 v7, v36, v38
	v_addc_co_u32_e32 v9, vcc, 0, v41, vcc
	global_store_dwordx4 v[8:9], v[4:7], off nt
	s_nop 1
	v_cvt_pk_bf16_f32 v4, v25, v27
	v_cvt_pk_bf16_f32 v5, v29, v31
	v_cvt_pk_bf16_f32 v6, v33, v35
	v_cvt_pk_bf16_f32 v7, v37, v39
	ds_read2_b32 v[8:9], v165 offset0:97 offset1:105
	ds_read2_b32 v[10:11], v165 offset0:162 offset1:170
	ds_read2_b32 v[12:13], v165 offset0:227 offset1:235
	ds_read2_b32 v[14:15], v48 offset0:36 offset1:44
	ds_read2_b32 v[16:17], v48 offset0:101 offset1:109
	ds_read2_b32 v[18:19], v48 offset0:166 offset1:174
	ds_read2_b32 v[20:21], v48 offset0:231 offset1:239
	ds_read2_b32 v[22:23], v165 offset0:32 offset1:40
	ds_read2_b32 v[24:25], v165 offset0:48 offset1:56
	ds_read2_b32 v[26:27], v165 offset0:113 offset1:121
	ds_read2_b32 v[28:29], v165 offset0:178 offset1:186
	ds_read2_b32 v[30:31], v165 offset0:243 offset1:251
	ds_read2_b32 v[32:33], v48 offset0:52 offset1:60
	ds_read2_b32 v[34:35], v48 offset0:117 offset1:125
	ds_read2_b32 v[36:37], v48 offset0:182 offset1:190
	ds_read2_b32 v[38:39], v48 offset0:247 offset1:255
	v_add_co_u32_e32 v48, vcc, s82, v40
	s_nop 1
	v_addc_co_u32_e32 v49, vcc, 0, v41, vcc
	global_store_dwordx4 v[48:49], v[4:7], off nt
	v_add_co_u32_e32 v48, vcc, s80, v40
	s_mov_b32 s40, 0x14000
	s_nop 0
	v_addc_co_u32_e32 v49, vcc, 0, v41, vcc
	s_waitcnt lgkmcnt(8)
	v_cvt_pk_bf16_f32 v4, v22, v8
	v_cvt_pk_bf16_f32 v5, v10, v12
	v_cvt_pk_bf16_f32 v6, v14, v16
	v_cvt_pk_bf16_f32 v7, v18, v20
	v_add_co_u32_e32 v8, vcc, s40, v40
	global_store_dwordx4 v[48:49], v[4:7], off nt
	s_nop 1
	v_cvt_pk_bf16_f32 v4, v23, v9
	v_cvt_pk_bf16_f32 v5, v11, v13
	v_cvt_pk_bf16_f32 v6, v15, v17
	v_cvt_pk_bf16_f32 v7, v19, v21
	v_addc_co_u32_e32 v9, vcc, 0, v41, vcc
	global_store_dwordx4 v[8:9], v[4:7], off nt
	v_add_co_u32_e32 v8, vcc, s83, v40
	s_waitcnt lgkmcnt(6)
	v_cvt_pk_bf16_f32 v4, v24, v26
	s_waitcnt lgkmcnt(4)
	v_cvt_pk_bf16_f32 v5, v28, v30
	s_waitcnt lgkmcnt(2)
	v_cvt_pk_bf16_f32 v6, v32, v34
	s_waitcnt lgkmcnt(0)
	v_cvt_pk_bf16_f32 v7, v36, v38
	v_addc_co_u32_e32 v9, vcc, 0, v41, vcc
	global_store_dwordx4 v[8:9], v[4:7], off nt
	v_add_co_u32_e32 v8, vcc, 0x1c000, v40
	s_nop 0
	v_cvt_pk_bf16_f32 v4, v25, v27
	v_cvt_pk_bf16_f32 v5, v29, v31
	v_cvt_pk_bf16_f32 v6, v33, v35
	v_cvt_pk_bf16_f32 v7, v37, v39
	v_addc_co_u32_e32 v9, vcc, 0, v41, vcc
	global_store_dwordx4 v[8:9], v[4:7], off nt

.LBB0_96:
	s_andn2_saveexec_b64 s[46:47], s[46:47]
	s_cbranch_execz .LBB0_98
	v_add_u32_e32 v4, 0xfffff930, v46
	v_lshrrev_b32_e32 v130, 7, v4
	v_lshl_add_u64 v[4:5], s[24:25], 0, v[130:131]
	v_readlane_b32 s48, v251, 35
	v_and_b32_e32 v47, 0x1c0, v3
	v_lshlrev_b64 v[4:5], 21, v[4:5]
	v_readlane_b32 s58, v251, 45
	v_readlane_b32 s59, v251, 46
	v_and_b32_e32 v76, 0x3c0, v43
	v_or_b32_e32 v7, v47, v123
	v_lshl_add_u64 v[4:5], s[58:59], 0, v[4:5]
	v_lshlrev_b64 v[40:41], 20, v[130:131]
	v_or_b32_e32 v6, v76, v162
	v_lshlrev_b32_e32 v130, 12, v7
	v_lshl_add_u64 v[4:5], v[4:5], 0, v[130:131]
	v_lshlrev_b32_e32 v130, 2, v6
	v_lshl_add_u64 v[68:69], v[4:5], 0, v[130:131]
	s_waitcnt lgkmcnt(0)
	v_add_co_u32_e32 v8, vcc, s88, v68
	s_mov_b32 s41, 0x8000
	s_nop 0
	v_addc_co_u32_e32 v9, vcc, 0, v69, vcc
	v_add_co_u32_e32 v12, vcc, s41, v68
	s_mov_b32 s42, 0xc000
	s_nop 0
	v_addc_co_u32_e32 v13, vcc, 0, v69, vcc
	v_add_co_u32_e32 v16, vcc, s42, v68
	s_mov_b32 s40, 0x14000
	s_nop 0
	v_addc_co_u32_e32 v17, vcc, 0, v69, vcc
	v_add_co_u32_e32 v20, vcc, s80, v68
	global_load_dwordx4 v[4:7], v[68:69], off nt
	s_nop 0
	global_load_dwordx4 v[8:11], v[8:9], off nt
	v_addc_co_u32_e32 v21, vcc, 0, v69, vcc
	v_add_co_u32_e32 v24, vcc, s40, v68
	s_mov_b32 s40, 0x1c000
	s_nop 0
	v_addc_co_u32_e32 v25, vcc, 0, v69, vcc
	v_add_co_u32_e32 v28, vcc, s83, v68
	global_load_dwordx4 v[12:15], v[12:13], off nt
	s_nop 0
	global_load_dwordx4 v[16:19], v[16:17], off nt
	v_addc_co_u32_e32 v29, vcc, 0, v69, vcc
	v_add_co_u32_e32 v32, vcc, s40, v68
	s_mov_b32 s40, 0x20000
	s_nop 0
	v_addc_co_u32_e32 v33, vcc, 0, v69, vcc
	v_add_co_u32_e32 v36, vcc, s40, v68
	s_mov_b32 s40, 0x24000
	s_nop 0
	v_addc_co_u32_e32 v37, vcc, 0, v69, vcc
	v_add_co_u32_e32 v48, vcc, s40, v68
	s_mov_b32 s40, 0x28000
	s_nop 0
	v_addc_co_u32_e32 v49, vcc, 0, v69, vcc
	v_add_co_u32_e32 v52, vcc, s40, v68
	s_mov_b32 s40, 0x2c000
	s_nop 0
	v_addc_co_u32_e32 v53, vcc, 0, v69, vcc
	v_add_co_u32_e32 v56, vcc, s40, v68
	s_mov_b32 s40, 0x30000
	s_nop 0
	v_addc_co_u32_e32 v57, vcc, 0, v69, vcc
	v_add_co_u32_e32 v60, vcc, s40, v68
	s_mov_b32 s40, 0x34000
	s_nop 0
	v_addc_co_u32_e32 v61, vcc, 0, v69, vcc
	v_add_co_u32_e32 v64, vcc, s40, v68
	s_mov_b32 s40, 0x38000
	s_nop 0
	v_addc_co_u32_e32 v65, vcc, 0, v69, vcc
	v_add_co_u32_e32 v70, vcc, s40, v68
	s_mov_b32 s40, 0x3c000
	s_nop 0
	v_addc_co_u32_e32 v71, vcc, 0, v69, vcc
	v_add_co_u32_e32 v72, vcc, s40, v68
	global_load_dwordx4 v[20:23], v[20:21], off nt
	s_nop 0
	global_load_dwordx4 v[24:27], v[24:25], off nt
	v_addc_co_u32_e32 v73, vcc, 0, v69, vcc
	global_load_dwordx4 v[28:31], v[28:29], off nt
	s_nop 0
	global_load_dwordx4 v[32:35], v[32:33], off nt
	s_nop 0
	global_load_dwordx4 v[36:39], v[36:37], off nt
	s_nop 0
	global_load_dwordx4 v[48:51], v[48:49], off nt
	s_nop 0
	global_load_dwordx4 v[52:55], v[52:53], off nt
	s_nop 0
	global_load_dwordx4 v[56:59], v[56:57], off nt
	s_nop 0
	global_load_dwordx4 v[60:63], v[60:61], off nt
	s_nop 0
	global_load_dwordx4 v[64:67], v[64:65], off nt
	s_nop 0
	global_load_dwordx4 v[68:71], v[70:71], off nt
	s_nop 0
	global_load_dwordx4 v[72:75], v[72:73], off nt
	v_readlane_b32 s60, v251, 47
	v_readlane_b32 s61, v251, 48
	v_readlane_b32 s54, v251, 41
	v_readlane_b32 s60, v255, 25
	s_movk_i32 s54, 0x1000
	v_readlane_b32 s61, v255, 26
	v_readlane_b32 s49, v251, 36
	v_readlane_b32 s50, v251, 37
	v_readlane_b32 s51, v251, 38
	v_readlane_b32 s52, v251, 39
	v_readlane_b32 s53, v251, 40
	v_readlane_b32 s55, v251, 42
	v_readlane_b32 s56, v251, 43
	v_readlane_b32 s57, v251, 44
	v_readlane_b32 s62, v251, 49
	v_readlane_b32 s63, v251, 50
	v_lshl_add_u64 v[40:41], s[34:35], 0, v[40:41]
	s_waitcnt vmcnt(0)
	ds_write2_b32 v163, v4, v5 offset1:1
	ds_write2_b32 v163, v6, v7 offset0:2 offset1:3
	v_add_u32_e32 v4, 0x410, v163
	ds_write2_b32 v4, v8, v9 offset1:1
	v_add_u32_e32 v4, 0x418, v163
	ds_write2_b32 v4, v10, v11 offset1:1
	v_add_u32_e32 v4, 0x820, v163
	ds_write2_b32 v4, v12, v13 offset1:1
	v_add_u32_e32 v4, 0x828, v163
	ds_write2_b32 v4, v14, v15 offset1:1
	v_add_u32_e32 v4, 0xc30, v163
	ds_write2_b32 v4, v16, v17 offset1:1
	v_add_u32_e32 v4, 0xc38, v163
	ds_write2_b32 v4, v18, v19 offset1:1
	v_add_u32_e32 v4, 0x1040, v163
	ds_write2_b32 v4, v20, v21 offset1:1
	v_add_u32_e32 v4, 0x1048, v163
	ds_write2_b32 v4, v22, v23 offset1:1
	v_add_u32_e32 v4, 0x1450, v163
	ds_write2_b32 v4, v24, v25 offset1:1
	v_add_u32_e32 v4, 0x1458, v163
	ds_write2_b32 v4, v26, v27 offset1:1
	v_add_u32_e32 v4, 0x1860, v163
	ds_write2_b32 v4, v28, v29 offset1:1
	v_add_u32_e32 v4, 0x1868, v163
	ds_write2_b32 v4, v30, v31 offset1:1
	v_add_u32_e32 v4, 0x1c70, v163
	ds_write2_b32 v4, v32, v33 offset1:1
	v_add_u32_e32 v4, 0x1c78, v163
	ds_write2_b32 v4, v34, v35 offset1:1
	v_add_u32_e32 v4, 0x2080, v163
	ds_write2_b32 v4, v36, v37 offset1:1
	v_add_u32_e32 v4, 0x2088, v163
	ds_write2_b32 v4, v38, v39 offset1:1
	v_add_u32_e32 v4, 0x2490, v163
	ds_write2_b32 v4, v48, v49 offset1:1
	v_add_u32_e32 v4, 0x2498, v163
	ds_write2_b32 v4, v50, v51 offset1:1
	v_add_u32_e32 v4, 0x28a0, v163
	ds_write2_b32 v4, v52, v53 offset1:1
	v_add_u32_e32 v4, 0x28a8, v163
	ds_write2_b32 v4, v54, v55 offset1:1
	v_add_u32_e32 v4, 0x2cb0, v163
	ds_write2_b32 v4, v56, v57 offset1:1
	v_add_u32_e32 v4, 0x2cb8, v163
	ds_write2_b32 v4, v58, v59 offset1:1
	v_add_u32_e32 v4, 0x30c0, v163
	ds_write2_b32 v4, v60, v61 offset1:1
	v_add_u32_e32 v4, 0x30c8, v163
	ds_write2_b32 v4, v62, v63 offset1:1
	v_add_u32_e32 v4, 0x34d0, v163
	ds_write2_b32 v4, v64, v65 offset1:1
	v_add_u32_e32 v4, 0x34d8, v163
	ds_write2_b32 v4, v66, v67 offset1:1
	v_add_u32_e32 v4, 0x38e0, v163
	ds_write2_b32 v4, v68, v69 offset1:1
	v_add_u32_e32 v4, 0x38e8, v163
	ds_write2_b32 v4, v70, v71 offset1:1
	v_add_u32_e32 v4, 0x3cf0, v163
	ds_write2_b32 v4, v72, v73 offset1:1
	v_add_u32_e32 v4, 0x3cf8, v163
	ds_write2_b32 v4, v74, v75 offset1:1
	v_add_u32_e32 v49, 0x400, v165
	ds_read2_b32 v[8:9], v165 offset0:65 offset1:73
	ds_read2_b32 v[10:11], v165 offset0:130 offset1:138
	ds_read2_b32 v[12:13], v165 offset0:195 offset1:203
	ds_read2_b32 v[14:15], v49 offset0:4 offset1:12
	ds_read2_b32 v[16:17], v49 offset0:69 offset1:77
	ds_read2_b32 v[18:19], v49 offset0:134 offset1:142
	ds_read2_b32 v[20:21], v49 offset0:199 offset1:207
	ds_read2_b32 v[22:23], v165 offset1:8
	ds_read2_b32 v[24:25], v165 offset0:16 offset1:24
	ds_read2_b32 v[26:27], v165 offset0:81 offset1:89
	ds_read2_b32 v[28:29], v165 offset0:146 offset1:154
	ds_read2_b32 v[30:31], v165 offset0:211 offset1:219
	ds_read2_b32 v[32:33], v49 offset0:20 offset1:28
	ds_read2_b32 v[34:35], v49 offset0:85 offset1:93
	ds_read2_b32 v[36:37], v49 offset0:150 offset1:158
	ds_read2_b32 v[38:39], v49 offset0:215 offset1:223
	v_lshlrev_b32_e32 v130, 1, v47
	v_lshl_add_u64 v[4:5], v[40:41], 0, v[130:131]
	v_lshlrev_b32_e32 v130, 1, v116
	v_or_b32_e32 v48, v76, v164
	v_lshl_add_u64 v[40:41], v[4:5], 0, v[130:131]
	v_lshlrev_b32_e32 v130, 10, v48
	v_lshl_add_u64 v[40:41], v[40:41], 0, v[130:131]
	s_waitcnt lgkmcnt(8)
	v_cvt_pk_bf16_f32 v4, v22, v8
	v_cvt_pk_bf16_f32 v5, v10, v12
	v_cvt_pk_bf16_f32 v6, v14, v16
	v_cvt_pk_bf16_f32 v7, v18, v20
	v_add_co_u32_e32 v8, vcc, s76, v40
	global_store_dwordx4 v[40:41], v[4:7], off nt
	s_nop 1
	v_cvt_pk_bf16_f32 v4, v23, v9
	v_cvt_pk_bf16_f32 v5, v11, v13
	v_cvt_pk_bf16_f32 v6, v15, v17
	v_cvt_pk_bf16_f32 v7, v19, v21
	v_addc_co_u32_e32 v9, vcc, 0, v41, vcc
	global_store_dwordx4 v[8:9], v[4:7], off nt
	v_add_co_u32_e32 v8, vcc, s88, v40
	s_waitcnt lgkmcnt(6)
	v_cvt_pk_bf16_f32 v4, v24, v26
	s_waitcnt lgkmcnt(4)
	v_cvt_pk_bf16_f32 v5, v28, v30
	s_waitcnt lgkmcnt(2)
	v_cvt_pk_bf16_f32 v6, v32, v34
	s_waitcnt lgkmcnt(0)
	v_cvt_pk_bf16_f32 v7, v36, v38
	v_addc_co_u32_e32 v9, vcc, 0, v41, vcc
	global_store_dwordx4 v[8:9], v[4:7], off nt
	v_add_co_u32_e32 v48, vcc, s75, v40
	s_nop 0
	v_cvt_pk_bf16_f32 v4, v25, v27
	v_cvt_pk_bf16_f32 v5, v29, v31
	v_cvt_pk_bf16_f32 v6, v33, v35
	v_cvt_pk_bf16_f32 v7, v37, v39
	ds_read2_b32 v[8:9], v165 offset0:97 offset1:105
	ds_read2_b32 v[10:11], v165 offset0:162 offset1:170
	ds_read2_b32 v[12:13], v165 offset0:227 offset1:235
	ds_read2_b32 v[14:15], v49 offset0:36 offset1:44
	ds_read2_b32 v[16:17], v49 offset0:101 offset1:109
	ds_read2_b32 v[18:19], v49 offset0:166 offset1:174
	ds_read2_b32 v[20:21], v49 offset0:231 offset1:239
	ds_read2_b32 v[22:23], v165 offset0:32 offset1:40
	ds_read2_b32 v[24:25], v165 offset0:48 offset1:56
	ds_read2_b32 v[26:27], v165 offset0:113 offset1:121
	ds_read2_b32 v[28:29], v165 offset0:178 offset1:186
	ds_read2_b32 v[30:31], v165 offset0:243 offset1:251
	ds_read2_b32 v[32:33], v49 offset0:52 offset1:60
	ds_read2_b32 v[34:35], v49 offset0:117 offset1:125
	ds_read2_b32 v[36:37], v49 offset0:182 offset1:190
	ds_read2_b32 v[38:39], v49 offset0:247 offset1:255
	v_addc_co_u32_e32 v49, vcc, 0, v41, vcc
	global_store_dwordx4 v[48:49], v[4:7], off nt
	v_add_co_u32_e32 v48, vcc, s41, v40
	s_mov_b32 s40, 0xa000
	s_nop 0
	v_addc_co_u32_e32 v49, vcc, 0, v41, vcc
	s_waitcnt lgkmcnt(8)
	v_cvt_pk_bf16_f32 v4, v22, v8
	v_cvt_pk_bf16_f32 v5, v10, v12
	v_cvt_pk_bf16_f32 v6, v14, v16
	v_cvt_pk_bf16_f32 v7, v18, v20
	v_add_co_u32_e32 v8, vcc, s40, v40
	global_store_dwordx4 v[48:49], v[4:7], off nt
	s_mov_b32 s77, 0x8000
	s_mov_b32 s82, 0xc000
	v_cvt_pk_bf16_f32 v4, v23, v9
	v_cvt_pk_bf16_f32 v5, v11, v13
	v_cvt_pk_bf16_f32 v6, v15, v17
	v_cvt_pk_bf16_f32 v7, v19, v21
	v_addc_co_u32_e32 v9, vcc, 0, v41, vcc
	global_store_dwordx4 v[8:9], v[4:7], off nt
	v_add_co_u32_e32 v8, vcc, s42, v40
	s_waitcnt lgkmcnt(6)
	v_cvt_pk_bf16_f32 v4, v24, v26
	s_waitcnt lgkmcnt(4)
	v_cvt_pk_bf16_f32 v5, v28, v30
	s_waitcnt lgkmcnt(2)
	v_cvt_pk_bf16_f32 v6, v32, v34
	s_waitcnt lgkmcnt(0)
	v_cvt_pk_bf16_f32 v7, v36, v38
	v_addc_co_u32_e32 v9, vcc, 0, v41, vcc
	global_store_dwordx4 v[8:9], v[4:7], off nt
	v_add_co_u32_e32 v8, vcc, 0xe000, v40
	s_nop 0
	v_cvt_pk_bf16_f32 v4, v25, v27
	v_cvt_pk_bf16_f32 v5, v29, v31
	v_cvt_pk_bf16_f32 v6, v33, v35
	v_cvt_pk_bf16_f32 v7, v37, v39
	v_addc_co_u32_e32 v9, vcc, 0, v41, vcc
	global_store_dwordx4 v[8:9], v[4:7], off nt

.LBB0_99:
	s_andn2_saveexec_b64 s[46:47], s[0:1]
	s_cbranch_execz .LBB0_84
	v_ashrrev_i32_e32 v4, 31, v46
	v_lshrrev_b32_e32 v4, 28, v4
	v_add_u32_e32 v4, v46, v4
	v_ashrrev_i32_e32 v47, 4, v4
	v_lshlrev_b32_e32 v77, 6, v47
	v_or_b32_e32 v6, v77, v162
	s_mov_b32 s0, 0xff93c000
	v_mad_u64_u32 v[4:5], s[0:1], v47, s0, v[2:3]
	v_cmp_gt_i32_e32 vcc, s33, v6
	v_ashrrev_i32_e32 v5, 31, v4
	v_lshl_add_u64 v[4:5], v[4:5], 2, s[22:23]
	v_cndmask_b32_e32 v6, 0, v6, vcc
	v_ashrrev_i32_e32 v7, 31, v6
	v_lshl_add_u64 v[40:41], v[6:7], 2, v[4:5]
	s_mov_b32 s0, 0x1b000
	s_waitcnt lgkmcnt(0)
	v_add_co_u32_e64 v8, s[0:1], s0, v40
	s_nop 1
	v_addc_co_u32_e64 v9, s[0:1], 0, v41, s[0:1]
	s_mov_b32 s0, 0x36000
	s_nop 0
	v_add_co_u32_e64 v12, s[0:1], s0, v40
	global_load_dwordx4 v[4:7], v[40:41], off nt
	s_nop 0
	global_load_dwordx4 v[8:11], v[8:9], off offset:256 nt
	v_addc_co_u32_e64 v13, s[0:1], 0, v41, s[0:1]
	s_mov_b32 s0, 0x51000
	s_nop 0
	v_add_co_u32_e64 v16, s[0:1], s0, v40
	s_nop 1
	v_addc_co_u32_e64 v17, s[0:1], 0, v41, s[0:1]
	s_mov_b32 s0, 0x6c000
	s_nop 0
	v_add_co_u32_e64 v20, s[0:1], s0, v40
	global_load_dwordx4 v[12:15], v[12:13], off offset:512 nt
	s_nop 0
	global_load_dwordx4 v[16:19], v[16:17], off offset:768 nt
	v_addc_co_u32_e64 v21, s[0:1], 0, v41, s[0:1]
	s_mov_b32 s0, 0x87000
	s_nop 0
	v_add_co_u32_e64 v24, s[0:1], s0, v40
	s_nop 1
	v_addc_co_u32_e64 v25, s[0:1], 0, v41, s[0:1]
	s_mov_b32 s0, 0xa2000
	s_nop 0
	v_add_co_u32_e64 v28, s[0:1], s0, v40
	global_load_dwordx4 v[20:23], v[20:21], off offset:1024 nt
	s_nop 0
	global_load_dwordx4 v[24:27], v[24:25], off offset:1280 nt
	v_addc_co_u32_e64 v29, s[0:1], 0, v41, s[0:1]
	s_mov_b32 s0, 0xbd000
	s_nop 0
	v_add_co_u32_e64 v32, s[0:1], s0, v40
	s_nop 1
	v_addc_co_u32_e64 v33, s[0:1], 0, v41, s[0:1]
	s_mov_b32 s0, 0xd8000
	s_nop 0
	v_add_co_u32_e64 v36, s[0:1], s0, v40
	global_load_dwordx4 v[28:31], v[28:29], off offset:1536 nt
	s_nop 0
	global_load_dwordx4 v[32:35], v[32:33], off offset:1792 nt
	v_addc_co_u32_e64 v37, s[0:1], 0, v41, s[0:1]
	s_mov_b32 s0, 0xf3000
	s_nop 0
	v_add_co_u32_e64 v48, s[0:1], s0, v40
	s_nop 1
	v_addc_co_u32_e64 v49, s[0:1], 0, v41, s[0:1]
	s_mov_b32 s0, 0x10e000
	s_nop 0
	v_add_co_u32_e64 v52, s[0:1], s0, v40
	global_load_dwordx4 v[36:39], v[36:37], off offset:2048 nt
	s_nop 0
	global_load_dwordx4 v[48:51], v[48:49], off offset:2304 nt
	v_addc_co_u32_e64 v53, s[0:1], 0, v41, s[0:1]
	s_mov_b32 s0, 0x129000
	s_nop 0
	v_add_co_u32_e64 v56, s[0:1], s0, v40
	s_nop 1
	v_addc_co_u32_e64 v57, s[0:1], 0, v41, s[0:1]
	s_mov_b32 s0, 0x144000
	s_nop 0
	v_add_co_u32_e64 v60, s[0:1], s0, v40
	global_load_dwordx4 v[52:55], v[52:53], off offset:2560 nt
	s_nop 0
	global_load_dwordx4 v[56:59], v[56:57], off offset:2816 nt
	v_addc_co_u32_e64 v61, s[0:1], 0, v41, s[0:1]
	s_mov_b32 s0, 0x15f000
	s_nop 0
	v_add_co_u32_e64 v64, s[0:1], s0, v40
	s_nop 1
	v_addc_co_u32_e64 v65, s[0:1], 0, v41, s[0:1]
	s_mov_b32 s0, 0x17a000
	s_nop 0
	v_add_co_u32_e64 v68, s[0:1], s0, v40
	global_load_dwordx4 v[60:63], v[60:61], off offset:3072 nt
	s_nop 0
	global_load_dwordx4 v[64:67], v[64:65], off offset:3328 nt
	v_addc_co_u32_e64 v69, s[0:1], 0, v41, s[0:1]
	s_mov_b32 s0, 0x195000
	s_nop 0
	v_add_co_u32_e64 v40, s[0:1], s0, v40
	s_nop 1
	v_addc_co_u32_e64 v41, s[0:1], 0, v41, s[0:1]
	global_load_dwordx4 v[68:71], v[68:69], off offset:3584 nt
	s_nop 0
	global_load_dwordx4 v[72:75], v[40:41], off offset:3840 nt
	v_lshlrev_b32_e32 v40, 10, v47
	v_sub_u32_e32 v76, v3, v40
	s_waitcnt vmcnt(0)
	v_cndmask_b32_e32 v4, 0, v4, vcc
	v_cndmask_b32_e32 v5, 0, v5, vcc
	ds_write2_b32 v163, v4, v5 offset1:1
	v_cndmask_b32_e32 v4, 0, v6, vcc
	v_cndmask_b32_e32 v5, 0, v7, vcc
	ds_write2_b32 v163, v4, v5 offset0:2 offset1:3
	v_cndmask_b32_e32 v4, 0, v8, vcc
	v_cndmask_b32_e32 v5, 0, v9, vcc
	v_add_u32_e32 v6, 0x410, v163
	ds_write2_b32 v6, v4, v5 offset1:1
	v_cndmask_b32_e32 v4, 0, v10, vcc
	v_cndmask_b32_e32 v5, 0, v11, vcc
	v_add_u32_e32 v6, 0x418, v163
	ds_write2_b32 v6, v4, v5 offset1:1
	v_cndmask_b32_e32 v4, 0, v12, vcc
	v_cndmask_b32_e32 v5, 0, v13, vcc
	v_add_u32_e32 v6, 0x820, v163
	ds_write2_b32 v6, v4, v5 offset1:1
	v_cndmask_b32_e32 v4, 0, v14, vcc
	v_cndmask_b32_e32 v5, 0, v15, vcc
	v_add_u32_e32 v6, 0x828, v163
	ds_write2_b32 v6, v4, v5 offset1:1
	v_cndmask_b32_e32 v4, 0, v16, vcc
	v_cndmask_b32_e32 v5, 0, v17, vcc
	v_add_u32_e32 v6, 0xc30, v163
	ds_write2_b32 v6, v4, v5 offset1:1
	v_cndmask_b32_e32 v4, 0, v18, vcc
	v_cndmask_b32_e32 v5, 0, v19, vcc
	v_add_u32_e32 v6, 0xc38, v163
	ds_write2_b32 v6, v4, v5 offset1:1
	v_cndmask_b32_e32 v4, 0, v20, vcc
	v_cndmask_b32_e32 v5, 0, v21, vcc
	v_add_u32_e32 v6, 0x1040, v163
	ds_write2_b32 v6, v4, v5 offset1:1
	v_cndmask_b32_e32 v4, 0, v22, vcc
	v_cndmask_b32_e32 v5, 0, v23, vcc
	v_add_u32_e32 v6, 0x1048, v163
	ds_write2_b32 v6, v4, v5 offset1:1
	v_cndmask_b32_e32 v4, 0, v24, vcc
	v_cndmask_b32_e32 v5, 0, v25, vcc
	v_add_u32_e32 v6, 0x1450, v163
	ds_write2_b32 v6, v4, v5 offset1:1
	v_cndmask_b32_e32 v4, 0, v26, vcc
	v_cndmask_b32_e32 v5, 0, v27, vcc
	v_add_u32_e32 v6, 0x1458, v163
	ds_write2_b32 v6, v4, v5 offset1:1
	v_cndmask_b32_e32 v4, 0, v28, vcc
	v_cndmask_b32_e32 v5, 0, v29, vcc
	v_add_u32_e32 v6, 0x1860, v163
	ds_write2_b32 v6, v4, v5 offset1:1
	v_cndmask_b32_e32 v4, 0, v30, vcc
	v_cndmask_b32_e32 v5, 0, v31, vcc
	v_add_u32_e32 v6, 0x1868, v163
	ds_write2_b32 v6, v4, v5 offset1:1
	v_cndmask_b32_e32 v4, 0, v32, vcc
	v_cndmask_b32_e32 v5, 0, v33, vcc
	v_add_u32_e32 v6, 0x1c70, v163
	ds_write2_b32 v6, v4, v5 offset1:1
	v_cndmask_b32_e32 v4, 0, v34, vcc
	v_cndmask_b32_e32 v5, 0, v35, vcc
	v_add_u32_e32 v6, 0x1c78, v163
	ds_write2_b32 v6, v4, v5 offset1:1
	v_cndmask_b32_e32 v4, 0, v36, vcc
	v_cndmask_b32_e32 v5, 0, v37, vcc
	v_add_u32_e32 v6, 0x2080, v163
	ds_write2_b32 v6, v4, v5 offset1:1
	v_cndmask_b32_e32 v4, 0, v38, vcc
	v_cndmask_b32_e32 v5, 0, v39, vcc
	v_add_u32_e32 v6, 0x2088, v163
	ds_write2_b32 v6, v4, v5 offset1:1
	v_cndmask_b32_e32 v4, 0, v48, vcc
	v_cndmask_b32_e32 v5, 0, v49, vcc
	v_add_u32_e32 v6, 0x2490, v163
	ds_write2_b32 v6, v4, v5 offset1:1
	v_cndmask_b32_e32 v4, 0, v50, vcc
	v_cndmask_b32_e32 v5, 0, v51, vcc
	v_add_u32_e32 v6, 0x2498, v163
	ds_write2_b32 v6, v4, v5 offset1:1
	v_cndmask_b32_e32 v4, 0, v52, vcc
	v_cndmask_b32_e32 v5, 0, v53, vcc
	v_add_u32_e32 v6, 0x28a0, v163
	ds_write2_b32 v6, v4, v5 offset1:1
	v_cndmask_b32_e32 v4, 0, v54, vcc
	v_cndmask_b32_e32 v5, 0, v55, vcc
	v_add_u32_e32 v6, 0x28a8, v163
	ds_write2_b32 v6, v4, v5 offset1:1
	v_cndmask_b32_e32 v4, 0, v56, vcc
	v_cndmask_b32_e32 v5, 0, v57, vcc
	v_add_u32_e32 v6, 0x2cb0, v163
	ds_write2_b32 v6, v4, v5 offset1:1
	v_cndmask_b32_e32 v4, 0, v58, vcc
	v_cndmask_b32_e32 v5, 0, v59, vcc
	v_add_u32_e32 v6, 0x2cb8, v163
	ds_write2_b32 v6, v4, v5 offset1:1
	v_cndmask_b32_e32 v4, 0, v60, vcc
	v_cndmask_b32_e32 v5, 0, v61, vcc
	v_add_u32_e32 v6, 0x30c0, v163
	ds_write2_b32 v6, v4, v5 offset1:1
	v_cndmask_b32_e32 v4, 0, v62, vcc
	v_cndmask_b32_e32 v5, 0, v63, vcc
	v_add_u32_e32 v6, 0x30c8, v163
	ds_write2_b32 v6, v4, v5 offset1:1
	v_cndmask_b32_e32 v4, 0, v64, vcc
	v_cndmask_b32_e32 v5, 0, v65, vcc
	v_add_u32_e32 v6, 0x34d0, v163
	ds_write2_b32 v6, v4, v5 offset1:1
	v_cndmask_b32_e32 v4, 0, v66, vcc
	v_cndmask_b32_e32 v5, 0, v67, vcc
	v_add_u32_e32 v6, 0x34d8, v163
	ds_write2_b32 v6, v4, v5 offset1:1
	v_cndmask_b32_e32 v4, 0, v68, vcc
	v_cndmask_b32_e32 v5, 0, v69, vcc
	v_add_u32_e32 v6, 0x38e0, v163
	ds_write2_b32 v6, v4, v5 offset1:1
	v_cndmask_b32_e32 v4, 0, v70, vcc
	v_cndmask_b32_e32 v5, 0, v71, vcc
	v_add_u32_e32 v6, 0x38e8, v163
	ds_write2_b32 v6, v4, v5 offset1:1
	v_cndmask_b32_e32 v4, 0, v72, vcc
	v_cndmask_b32_e32 v5, 0, v73, vcc
	v_add_u32_e32 v6, 0x3cf0, v163
	ds_write2_b32 v6, v4, v5 offset1:1
	v_cndmask_b32_e32 v4, 0, v74, vcc
	v_cndmask_b32_e32 v5, 0, v75, vcc
	v_add_u32_e32 v6, 0x3cf8, v163
	ds_write2_b32 v6, v4, v5 offset1:1
	v_add_u32_e32 v40, 0x400, v165
	ds_read2_b32 v[24:25], v165 offset1:8
	ds_read2_b32 v[26:27], v165 offset0:65 offset1:73
	ds_read2_b32 v[28:29], v165 offset0:130 offset1:138
	ds_read2_b32 v[30:31], v165 offset0:195 offset1:203
	ds_read2_b32 v[32:33], v40 offset0:4 offset1:12
	ds_read2_b32 v[34:35], v40 offset0:69 offset1:77
	ds_read2_b32 v[36:37], v40 offset0:134 offset1:142
	ds_read2_b32 v[38:39], v40 offset0:199 offset1:207
	ds_read2_b32 v[8:9], v165 offset0:16 offset1:24
	ds_read2_b32 v[10:11], v165 offset0:81 offset1:89
	ds_read2_b32 v[12:13], v165 offset0:146 offset1:154
	ds_read2_b32 v[14:15], v165 offset0:211 offset1:219
	ds_read2_b32 v[16:17], v40 offset0:20 offset1:28
	ds_read2_b32 v[18:19], v40 offset0:85 offset1:93
	ds_read2_b32 v[20:21], v40 offset0:150 offset1:158
	ds_read2_b32 v[22:23], v40 offset0:215 offset1:223
	v_or_b32_e32 v6, v77, v164
	v_ashrrev_i32_e32 v77, 31, v76
	v_lshl_add_u64 v[4:5], v[76:77], 1, v[120:121]
	v_cmp_gt_i32_e32 vcc, s33, v6
	s_and_saveexec_b64 s[0:1], vcc
	s_cbranch_execz .LBB0_102
	v_ashrrev_i32_e32 v7, 31, v6
	v_lshlrev_b64 v[52:53], 11, v[6:7]
	s_waitcnt lgkmcnt(14)
	v_cvt_pk_bf16_f32 v48, v24, v26
	s_waitcnt lgkmcnt(12)
	v_cvt_pk_bf16_f32 v49, v28, v30
	s_waitcnt lgkmcnt(10)
	v_cvt_pk_bf16_f32 v50, v32, v34
	s_waitcnt lgkmcnt(8)
	v_cvt_pk_bf16_f32 v51, v36, v38
	v_lshl_add_u64 v[52:53], v[4:5], 0, v[52:53]
	global_store_dwordx4 v[52:53], v[48:51], off nt
.LBB0_102:
	s_or_b64 exec, exec, s[0:1]
	s_waitcnt lgkmcnt(14)
	v_or_b32_e32 v24, 8, v6
	v_cmp_gt_i32_e32 vcc, s33, v24
	s_and_saveexec_b64 s[0:1], vcc
	s_cbranch_execz .LBB0_104
	v_cvt_pk_bf16_f32 v26, v25, v27
	v_ashrrev_i32_e32 v25, 31, v24
	v_lshlrev_b64 v[24:25], 11, v[24:25]
	s_waitcnt lgkmcnt(12)
	v_cvt_pk_bf16_f32 v27, v29, v31
	s_waitcnt lgkmcnt(10)
	v_cvt_pk_bf16_f32 v28, v33, v35
	s_waitcnt lgkmcnt(8)
	v_cvt_pk_bf16_f32 v29, v37, v39
	v_lshl_add_u64 v[24:25], v[4:5], 0, v[24:25]
	global_store_dwordx4 v[24:25], v[26:29], off nt
.LBB0_104:
	s_or_b64 exec, exec, s[0:1]
	v_or_b32_e32 v24, 16, v6
	v_cmp_gt_i32_e32 vcc, s33, v24
	s_and_saveexec_b64 s[0:1], vcc
	s_cbranch_execz .LBB0_106
	v_ashrrev_i32_e32 v25, 31, v24
	v_lshlrev_b64 v[24:25], 11, v[24:25]
	s_waitcnt lgkmcnt(6)
	v_cvt_pk_bf16_f32 v26, v8, v10
	s_waitcnt lgkmcnt(4)
	v_cvt_pk_bf16_f32 v27, v12, v14
	s_waitcnt lgkmcnt(2)
	v_cvt_pk_bf16_f32 v28, v16, v18
	s_waitcnt lgkmcnt(0)
	v_cvt_pk_bf16_f32 v29, v20, v22
	v_lshl_add_u64 v[24:25], v[4:5], 0, v[24:25]
	global_store_dwordx4 v[24:25], v[26:29], off nt
.LBB0_106:
	s_or_b64 exec, exec, s[0:1]
	s_waitcnt lgkmcnt(7)
	v_or_b32_e32 v8, 24, v6
	v_cmp_gt_i32_e32 vcc, s33, v8
	s_and_saveexec_b64 s[0:1], vcc
	s_cbranch_execz .LBB0_108
	s_waitcnt lgkmcnt(6)
	v_cvt_pk_bf16_f32 v10, v9, v11
	v_ashrrev_i32_e32 v9, 31, v8
	v_lshlrev_b64 v[8:9], 11, v[8:9]
	s_waitcnt lgkmcnt(4)
	v_cvt_pk_bf16_f32 v11, v13, v15
	s_waitcnt lgkmcnt(2)
	v_cvt_pk_bf16_f32 v12, v17, v19
	s_waitcnt lgkmcnt(0)
	v_cvt_pk_bf16_f32 v13, v21, v23
	v_lshl_add_u64 v[8:9], v[4:5], 0, v[8:9]
	global_store_dwordx4 v[8:9], v[10:13], off nt
.LBB0_108:
	s_or_b64 exec, exec, s[0:1]
	ds_read2_b32 v[24:25], v165 offset0:32 offset1:40
	ds_read2_b32 v[26:27], v165 offset0:97 offset1:105
	ds_read2_b32 v[28:29], v165 offset0:162 offset1:170
	ds_read2_b32 v[30:31], v165 offset0:227 offset1:235
	ds_read2_b32 v[32:33], v40 offset0:36 offset1:44
	ds_read2_b32 v[34:35], v40 offset0:101 offset1:109
	ds_read2_b32 v[36:37], v40 offset0:166 offset1:174
	ds_read2_b32 v[38:39], v40 offset0:231 offset1:239
	ds_read2_b32 v[8:9], v165 offset0:48 offset1:56
	s_waitcnt lgkmcnt(14)
	ds_read2_b32 v[10:11], v165 offset0:113 offset1:121
	ds_read2_b32 v[12:13], v165 offset0:178 offset1:186
	s_waitcnt lgkmcnt(14)
	ds_read2_b32 v[14:15], v165 offset0:243 offset1:251
	ds_read2_b32 v[16:17], v40 offset0:52 offset1:60
	s_waitcnt lgkmcnt(14)
	ds_read2_b32 v[18:19], v40 offset0:117 offset1:125
	ds_read2_b32 v[20:21], v40 offset0:182 offset1:190
	s_waitcnt lgkmcnt(14)
	ds_read2_b32 v[22:23], v40 offset0:247 offset1:255
	v_or_b32_e32 v40, 32, v6
	v_cmp_gt_i32_e32 vcc, s33, v40
	s_and_saveexec_b64 s[0:1], vcc
	s_cbranch_execz .LBB0_110
	v_ashrrev_i32_e32 v41, 31, v40
	v_lshlrev_b64 v[40:41], 11, v[40:41]
	s_waitcnt lgkmcnt(14)
	v_cvt_pk_bf16_f32 v48, v24, v26
	s_waitcnt lgkmcnt(12)
	v_cvt_pk_bf16_f32 v49, v28, v30
	s_waitcnt lgkmcnt(10)
	v_cvt_pk_bf16_f32 v50, v32, v34
	s_waitcnt lgkmcnt(8)
	v_cvt_pk_bf16_f32 v51, v36, v38
	v_lshl_add_u64 v[40:41], v[4:5], 0, v[40:41]
	global_store_dwordx4 v[40:41], v[48:51], off nt
.LBB0_110:
	s_or_b64 exec, exec, s[0:1]
	v_or_b32_e32 v24, 40, v6
	v_cmp_gt_i32_e32 vcc, s33, v24
	s_and_saveexec_b64 s[0:1], vcc
	s_cbranch_execz .LBB0_112
	s_waitcnt lgkmcnt(14)
	v_cvt_pk_bf16_f32 v26, v25, v27
	v_ashrrev_i32_e32 v25, 31, v24
	v_lshlrev_b64 v[24:25], 11, v[24:25]
	s_waitcnt lgkmcnt(12)
	v_cvt_pk_bf16_f32 v27, v29, v31
	s_waitcnt lgkmcnt(10)
	v_cvt_pk_bf16_f32 v28, v33, v35
	s_waitcnt lgkmcnt(8)
	v_cvt_pk_bf16_f32 v29, v37, v39
	v_lshl_add_u64 v[24:25], v[4:5], 0, v[24:25]
	global_store_dwordx4 v[24:25], v[26:29], off nt
.LBB0_112:
	s_or_b64 exec, exec, s[0:1]
	v_or_b32_e32 v24, 48, v6
	v_cmp_gt_i32_e32 vcc, s33, v24
	s_and_saveexec_b64 s[0:1], vcc
	s_cbranch_execz .LBB0_114
	v_ashrrev_i32_e32 v25, 31, v24
	v_lshlrev_b64 v[24:25], 11, v[24:25]
	s_waitcnt lgkmcnt(6)
	v_cvt_pk_bf16_f32 v26, v8, v10
	s_waitcnt lgkmcnt(4)
	v_cvt_pk_bf16_f32 v27, v12, v14
	s_waitcnt lgkmcnt(2)
	v_cvt_pk_bf16_f32 v28, v16, v18
	s_waitcnt lgkmcnt(0)
	v_cvt_pk_bf16_f32 v29, v20, v22
	v_lshl_add_u64 v[24:25], v[4:5], 0, v[24:25]
	global_store_dwordx4 v[24:25], v[26:29], off nt
.LBB0_114:
	s_or_b64 exec, exec, s[0:1]
	v_or_b32_e32 v6, 56, v6
	v_cmp_gt_i32_e32 vcc, s33, v6
	s_and_saveexec_b64 s[0:1], vcc
	s_cbranch_execz .LBB0_83
	v_ashrrev_i32_e32 v7, 31, v6
	v_lshlrev_b64 v[6:7], 11, v[6:7]
	s_waitcnt lgkmcnt(6)
	v_cvt_pk_bf16_f32 v8, v9, v11
	s_waitcnt lgkmcnt(4)
	v_cvt_pk_bf16_f32 v9, v13, v15
	s_waitcnt lgkmcnt(2)
	v_cvt_pk_bf16_f32 v10, v17, v19
	s_waitcnt lgkmcnt(0)
	v_cvt_pk_bf16_f32 v11, v21, v23
	v_lshl_add_u64 v[4:5], v[4:5], 0, v[6:7]
	global_store_dwordx4 v[4:5], v[8:11], off nt
	s_branch .LBB0_83
